# speedup vs baseline: 1.0116x; 1.0116x over previous
.LBB1_43:
	s_mov_b32 s46, 0
	s_and_b64 s[72:73], exec, s[6:7]
	s_cbranch_scc1 .Lpf_skip_0
	ds_read_b128 v[250:253], v199 offset:9216
	ds_read_b128 v[120:123], v198 offset:57600
	ds_read_b128 v[124:127], v199 offset:9344
	ds_read_b128 v[246:249], v199 offset:9280
	ds_read_b128 v[128:131], v199 offset:9408
.Lpf_skip_0:
	s_waitcnt lgkmcnt(0)
	s_barrier
	ds_read_b128 v[146:149], v193
	ds_read_b128 v[142:145], v193 offset:64
	ds_read_b128 v[138:141], v193 offset:128
	ds_read_b128 v[134:137], v193 offset:192
	v_and_or_b32 v233, s33, 64, v189
	s_and_saveexec_b64 s[24:25], s[6:7]
	s_xor_b64 s[24:25], exec, s[24:25]
	s_cbranch_execz .LBB1_55
	s_and_saveexec_b64 s[42:43], s[8:9]
	s_xor_b64 s[42:43], exec, s[42:43]
	s_cbranch_execz .LBB1_52
	s_cmpk_eq_i32 s40, 0x1810
	s_cbranch_scc1 .LBB1_49
	v_lshl_add_u64 v[116:117], v[160:161], 0, s[40:41]
	global_load_dword v188, v[116:117], off offset:560 nt
	global_load_dword v187, v[116:117], off offset:700 nt
	global_load_dword v186, v[116:117], off offset:840 nt
	global_load_dword v157, v[116:117], off offset:980 nt
	s_and_saveexec_b64 s[44:45], s[26:27]
	s_cbranch_execz .LBB1_48
	v_lshl_add_u64 v[116:117], v[158:159], 0, s[40:41]
	global_load_dword v155, v[116:117], off offset:560 nt
	global_load_dword v182, v[116:117], off offset:700 nt
	global_load_dword v183, v[116:117], off offset:840 nt
	global_load_dword v184, v[116:117], off offset:980 nt

.LBB1_55:
	s_or_saveexec_b64 s[24:25], s[24:25]
	v_mov_b32_e32 v116, 0
	v_lshlrev_b32_e32 v234, 1, v190
	v_lshlrev_b32_e32 v235, 1, v191
	v_mov_b32_e32 v117, 0
	v_mov_b32_e32 v166, 0
	v_mov_b32_e32 v167, 0
	v_mov_b32_e32 v150, 0
	v_mov_b32_e32 v151, 0
	v_mov_b32_e32 v152, 0
	v_mov_b32_e32 v153, 0
	v_mov_b32_e32 v174, 0
	v_mov_b32_e32 v175, 0
	v_mov_b32_e32 v172, 0
	v_mov_b32_e32 v173, 0
	s_xor_b64 exec, exec, s[24:25]
	s_cbranch_execz .LBB1_57
	s_lshl_b32 s42, s46, 1
	v_add_u32_e32 v115, s42, v199
	v_mad_u32_u24 v176, v233, s3, v227
	v_mov_b32_e32 v115, s54
	v_mad_u32_u24 v162, v233, s53, v115
	v_add3_u32 v115, v162, v234, v235
	ds_read_b64 v[132:133], v115 offset:80
	v_mad_u32_u24 v115, v233, s52, v198
	ds_read_b128 v[150:153], v115 offset:60416
	v_mov_b32_e32 v115, s56
	s_waitcnt lgkmcnt(5)
	v_mfma_f32_16x16x32_bf16 v[240:243], v[86:89], v[146:149], 0
	s_waitcnt lgkmcnt(2)
	v_mfma_f32_16x16x32_bf16 v[124:127], v[124:127], v[138:141], 0
	v_mfma_f32_16x16x32_bf16 v[116:119], v[250:253], v[146:149], v[120:123]
	v_mfma_f32_16x16x32_bf16 v[118:121], v[246:249], v[142:145], v[116:119]
	v_mfma_f32_16x16x32_bf16 v[122:125], v[128:131], v[134:137], v[124:127]
	s_nop 0
	s_waitcnt lgkmcnt(1)
	v_lshlrev_b32_e32 v116, 16, v132
	v_and_b32_e32 v117, 0xffff0000, v132
	v_lshlrev_b32_e32 v166, 16, v133
	v_and_b32_e32 v167, 0xffff0000, v133
	s_nop 2
	v_pk_add_f32 v[172:173], v[120:121], v[124:125]
	v_pk_add_f32 v[174:175], v[118:119], v[122:123]
	v_sub_f32_e32 v119, 1.0, v117
	v_sub_f32_e32 v118, 1.0, v116
	v_sub_f32_e32 v121, 1.0, v167
	v_sub_f32_e32 v120, 1.0, v166
	v_pk_mul_f32 v[120:121], v[172:173], v[120:121]
	v_pk_mul_f32 v[118:119], v[174:175], v[118:119]
	s_waitcnt lgkmcnt(0)
	v_pk_fma_f32 v[122:123], v[152:153], v[166:167], v[120:121]
	v_pk_fma_f32 v[124:125], v[150:151], v[116:117], v[118:119]
	v_mfma_f32_16x16x32_bf16 v[118:121], v[2:5], v[146:149], 0
	v_cndmask_b32_e64 v115, v123, v115, s[14:15]
	v_cndmask_b32_e64 v123, v122, v122, s[14:15]
	v_cndmask_b32_e64 v122, v125, v125, s[14:15]
	v_cndmask_b32_e64 v124, v124, v124, s[14:15]
	v_cvt_pk_bf16_f32 v122, v124, v122
	v_cvt_pk_bf16_f32 v123, v123, v115
	ds_write_b64 v200, v[122:123] offset:58112
	s_and_saveexec_b64 s[72:73], s[18:19]
	v_mov_b32_e32 v115, 0xe380
	ds_add_u32 v115, v115
	s_or_b64 exec, exec, s[72:73]
	v_mfma_f32_16x16x32_bf16 v[118:121], v[6:9], v[142:145], v[118:121]
	v_lshl_add_u32 v115, v192, 1, v162
	ds_read_b128 v[130:133], v115 offset:128
	ds_read_b128 v[236:239], v176 offset:2304
	v_add_u32_e32 v115, s42, v228
	ds_read_b128 v[162:165], v115 offset:39168
	ds_read_b128 v[244:247], v115 offset:39232
	v_mfma_f32_16x16x32_bf16 v[118:121], v[10:13], v[138:141], v[118:121]
	v_mfma_f32_16x16x32_bf16 v[118:121], v[14:17], v[134:137], v[118:121]
	s_waitcnt lgkmcnt(1)
	v_mfma_f32_16x16x32_bf16 v[162:165], v[162:165], v[236:239], 0
	ds_read_b128 v[236:239], v176 offset:2368
	v_mfma_f32_16x16x32_bf16 v[126:129], v[26:29], v[130:133], v[118:121]
	v_mfma_f32_16x16x32_bf16 v[118:121], v[30:33], v[146:149], 0
	v_mfma_f32_16x16x32_bf16 v[122:125], v[58:61], v[146:149], 0
	v_mfma_f32_16x16x32_bf16 v[118:121], v[34:37], v[142:145], v[118:121]
	v_mfma_f32_16x16x32_bf16 v[122:125], v[62:65], v[142:145], v[122:125]
	s_waitcnt lgkmcnt(0)
	v_mfma_f32_16x16x32_bf16 v[162:165], v[244:247], v[236:239], v[162:165]
	v_mov_b32_e32 v246, 0xe380
	ds_read_b32 v246, v246
	v_mfma_f32_16x16x32_bf16 v[236:239], v[90:93], v[142:145], v[240:243]
	v_mfma_f32_16x16x32_bf16 v[118:121], v[38:41], v[138:141], v[118:121]
	s_nop 5
	v_med3_f32 v115, v162, s55, 0
	v_exp_f32_e32 v162, v115
	v_med3_f32 v115, v163, s55, 0
	v_mfma_f32_16x16x32_bf16 v[122:125], v[66:69], v[138:141], v[122:125]
	v_exp_f32_e32 v163, v115
	v_med3_f32 v115, v164, s55, 0
	v_exp_f32_e32 v164, v115
	v_mfma_f32_16x16x32_bf16 v[236:239], v[94:97], v[138:141], v[236:239]
	v_med3_f32 v115, v165, s55, 0
	v_exp_f32_e32 v165, v115
	v_mfma_f32_16x16x32_bf16 v[118:121], v[42:45], v[134:137], v[118:121]
	v_mfma_f32_16x16x32_bf16 v[122:125], v[70:73], v[134:137], v[122:125]
	v_mfma_f32_16x16x32_bf16 v[236:239], v[98:101], v[134:137], v[236:239]
	v_mfma_f32_16x16x32_bf16 v[118:121], v[54:57], v[130:133], v[118:121]
	v_mfma_f32_16x16x32_bf16 v[122:125], v[82:85], v[130:133], v[122:125]
	v_mfma_f32_16x16x32_bf16 v[130:133], v[110:113], v[130:133], v[236:239]

.Lred_skip_0:
	s_nop 5
	v_exp_f32_e32 v115, v116
	v_med3_f32 v116, v120, s55, v232
	v_exp_f32_e32 v125, v116
	v_mfma_f32_16x16x32_bf16 v[130:133], v[102:105], v[134:137], v[130:133]
	v_med3_f32 v121, v121, s55, v232
	v_exp_f32_e32 v124, v126
	v_exp_f32_e32 v126, v127
	v_exp_f32_e32 v127, v121
	v_mfma_f32_16x16x32_bf16 v[130:133], v[106:109], v[138:141], v[130:133]
	v_exp_f32_e32 v117, v117
	v_add_f32_e32 v115, 1.0, v115
	v_pk_add_f32 v[134:135], v[124:125], 1.0 op_sel_hi:[1,0]
	v_rcp_f32_e32 v120, v115
	v_mul_f32_e32 v115, v134, v135
	v_pk_add_f32 v[134:135], v[126:127], 1.0 op_sel_hi:[1,0]
	s_nop 1
	v_exp_f32_e32 v116, v130
	v_rcp_f32_e32 v130, v115
	v_add_f32_e32 v115, 1.0, v117
	v_mul_f32_e32 v117, v134, v135
	v_exp_f32_e32 v124, v131
	v_rcp_f32_e32 v131, v117
	v_rcp_f32_e32 v121, v115
	v_mov_b32_e32 v126, v125
	v_pk_add_f32 v[126:127], v[126:127], 1.0 op_sel_hi:[1,0] neg_lo:[1,0] neg_hi:[1,0]
	v_med3_f32 v123, v123, s55, v232
	v_pk_mul_f32 v[126:127], v[126:127], v[130:131]
	v_exp_f32_e32 v119, v119
	v_pk_fma_f32 v[168:169], v[168:169], v[120:121], v[126:127]
	s_nop 0
	v_mul_f32_e32 v115, 0xc038aa3b, v168
	v_med3_f32 v115, v115, s55, v232
	v_exp_f32_e32 v117, v115
	v_mul_f32_e32 v115, 0xc038aa3b, v169
	v_med3_f32 v115, v115, s55, v232
	v_exp_f32_e32 v125, v115
	v_pk_add_f32 v[120:121], v[116:117], 1.0 op_sel_hi:[1,0]
	v_pk_add_f32 v[126:127], v[124:125], 1.0 op_sel_hi:[1,0]
	v_mul_f32_e32 v115, v120, v121
	v_rcp_f32_e32 v120, v115
	v_mul_f32_e32 v115, v126, v127
	v_rcp_f32_e32 v121, v115
	v_mov_b32_e32 v124, v117
	v_exp_f32_e32 v115, v118
	v_med3_f32 v118, v122, s55, v232
	v_pk_add_f32 v[116:117], v[124:125], 1.0 op_sel_hi:[1,0] neg_lo:[1,0] neg_hi:[1,0]
	v_exp_f32_e32 v124, v128
	v_exp_f32_e32 v125, v118
	v_add_f32_e32 v115, 1.0, v115
	v_rcp_f32_e32 v122, v115
	v_exp_f32_e32 v118, v132
	v_pk_add_f32 v[126:127], v[124:125], 1.0 op_sel_hi:[1,0]
	v_exp_f32_e32 v124, v133
	v_mul_f32_e32 v115, v126, v127
	v_exp_f32_e32 v126, v129
	v_exp_f32_e32 v127, v123
	v_rcp_f32_e32 v128, v115
	v_add_f32_e32 v115, 1.0, v119
	v_rcp_f32_e32 v123, v115
	v_pk_add_f32 v[130:131], v[126:127], 1.0 op_sel_hi:[1,0]
	v_mov_b32_e32 v126, v125
	v_mul_f32_e32 v119, v130, v131
	v_rcp_f32_e32 v129, v119
	v_pk_add_f32 v[126:127], v[126:127], 1.0 op_sel_hi:[1,0] neg_lo:[1,0] neg_hi:[1,0]
	v_pk_mul_f32 v[116:117], v[116:117], v[120:121]
	v_pk_mul_f32 v[126:127], v[126:127], v[128:129]
	s_nop 0
	v_pk_fma_f32 v[170:171], v[170:171], v[122:123], v[126:127]
	v_cvt_pk_bf16_f32 v120, v116, v117
	v_mul_f32_e32 v115, 0xc038aa3b, v170
	v_med3_f32 v115, v115, s55, v232
	v_exp_f32_e32 v119, v115
	v_mul_f32_e32 v115, 0xc038aa3b, v171
	v_med3_f32 v115, v115, s55, v232
	v_exp_f32_e32 v125, v115
	v_pk_add_f32 v[122:123], v[118:119], 1.0 op_sel_hi:[1,0]
	v_pk_mul_f32 v[116:117], v[162:163], v[116:117]
	v_mul_f32_e32 v115, v122, v123
	v_pk_add_f32 v[126:127], v[124:125], 1.0 op_sel_hi:[1,0]
	v_rcp_f32_e32 v122, v115
	v_mul_f32_e32 v115, v126, v127
	v_rcp_f32_e32 v123, v115
	v_mov_b32_e32 v124, v119
	v_pk_add_f32 v[118:119], v[124:125], 1.0 op_sel_hi:[1,0] neg_lo:[1,0] neg_hi:[1,0]
	v_cvt_pk_bf16_f32 v116, v116, v117
	v_pk_mul_f32 v[118:119], v[118:119], v[122:123]
	v_lshl_add_u64 v[122:123], v[166:167], 1, s[30:31]
	v_cvt_pk_bf16_f32 v121, v118, v119
	v_pk_mul_f32 v[118:119], v[164:165], v[118:119]
	global_store_dwordx2 v[122:123], v[120:121], off nt
	v_cvt_pk_bf16_f32 v117, v118, v119
	ds_write_b64 v205, v[116:117] offset:4608
	s_and_b64 s[72:73], exec, s[6:7]
	s_cbranch_scc1 .Lpf_skip_1
	ds_read_b128 v[250:253], v199 offset:9216
	ds_read_b128 v[120:123], v198 offset:57600
	ds_read_b128 v[124:127], v199 offset:9344
	ds_read_b128 v[246:249], v199 offset:9280
	ds_read_b128 v[128:131], v199 offset:9408
.Lpf_skip_1:
	s_waitcnt lgkmcnt(0)
	s_barrier
	ds_read_b128 v[146:149], v206 offset:4608
	ds_read_b128 v[142:145], v206 offset:4672
	ds_read_b128 v[138:141], v206 offset:4736
	ds_read_b128 v[134:137], v206 offset:4800
	v_or_b32_e32 v167, 16, v233
	s_and_saveexec_b64 s[24:25], s[6:7]
	s_xor_b64 s[24:25], exec, s[24:25]
	s_cbranch_execz .LBB1_91
	s_and_saveexec_b64 s[42:43], s[8:9]
	s_xor_b64 s[42:43], exec, s[42:43]
	s_cbranch_execz .LBB1_88
	s_cmpk_eq_i32 s40, 0x1810
	s_cbranch_scc1 .LBB1_88
	s_waitcnt vmcnt(4)
	v_fma_f32 v115, v188, v178, v179
	v_max_f32_e32 v115, 0, v115
	v_mul_f32_e32 v115, 0xbfb8aa3b, v115
	v_exp_f32_e32 v115, v115
	s_bitcmp1_b32 s59, 0
	s_waitcnt vmcnt(3)
	v_fma_f32 v116, v178, v187, v179
	s_cselect_b32 s47, 0, 0x1200
	v_cvt_pk_bf16_f32 v115, v115, s0
	ds_write_b16 v213, v115
	v_max_f32_e32 v115, 0, v116
	v_cvt_pk_bf16_f32 v116, v188, s0
	v_lshl_add_u32 v117, s47, 1, v221
	v_mul_f32_e32 v115, 0xbfb8aa3b, v115
	ds_write_b16 v117, v116
	s_waitcnt vmcnt(2)
	v_fma_f32 v116, v178, v186, v179
	v_exp_f32_e32 v115, v115
	v_max_f32_e32 v116, 0, v116
	v_mul_f32_e32 v116, 0xbfb8aa3b, v116
	v_exp_f32_e32 v116, v116
	v_cvt_pk_bf16_f32 v115, v115, s0
	ds_write_b16 v213, v115 offset:3584
	v_cvt_pk_bf16_f32 v115, v187, s0
	ds_write_b16 v117, v115 offset:2304
	v_cvt_pk_bf16_f32 v115, v116, s0
	s_waitcnt vmcnt(1)
	v_fma_f32 v116, v178, v157, v179
	v_max_f32_e32 v116, 0, v116
	v_mul_f32_e32 v116, 0xbfb8aa3b, v116
	v_exp_f32_e32 v116, v116
	ds_write_b16 v213, v115 offset:7168
	v_cvt_pk_bf16_f32 v115, v186, s0
	ds_write_b16 v117, v115 offset:4608
	v_cvt_pk_bf16_f32 v115, v116, s0
	ds_write_b16 v213, v115 offset:10752
	v_cvt_pk_bf16_f32 v115, v157, s0
	ds_write_b16 v117, v115 offset:6912
	s_and_saveexec_b64 s[44:45], s[26:27]
	s_cbranch_execz .LBB1_85
	v_fma_f32 v115, v155, v180, v181
	v_max_f32_e32 v115, 0, v115
	v_mul_f32_e32 v115, 0xbfb8aa3b, v115
	v_exp_f32_e32 v115, v115
	v_fma_f32 v116, v180, v182, v181
	v_max_f32_e32 v116, 0, v116
	v_mul_f32_e32 v116, 0xbfb8aa3b, v116
	v_cvt_pk_bf16_f32 v115, v115, s0
	ds_write_b16 v214, v115
	v_exp_f32_e32 v115, v116
	v_cvt_pk_bf16_f32 v116, v155, s0
	v_lshl_add_u32 v117, s47, 1, v222
	ds_write_b16 v117, v116
	v_fma_f32 v116, v180, v183, v181
	v_max_f32_e32 v116, 0, v116
	v_mul_f32_e32 v116, 0xbfb8aa3b, v116
	v_exp_f32_e32 v116, v116
	v_cvt_pk_bf16_f32 v115, v115, s0
	ds_write_b16 v214, v115 offset:3584
	v_cvt_pk_bf16_f32 v115, v182, s0
	ds_write_b16 v117, v115 offset:2304
	v_cvt_pk_bf16_f32 v115, v116, s0
	v_fma_f32 v116, v180, v184, v181
	v_max_f32_e32 v116, 0, v116
	v_mul_f32_e32 v116, 0xbfb8aa3b, v116
	v_exp_f32_e32 v116, v116
	ds_write_b16 v214, v115 offset:7168
	v_cvt_pk_bf16_f32 v115, v183, s0
	ds_write_b16 v117, v115 offset:4608
	v_cvt_pk_bf16_f32 v115, v116, s0
	ds_write_b16 v214, v115 offset:10752
	v_cvt_pk_bf16_f32 v115, v184, s0
	ds_write_b16 v117, v115 offset:6912

.LBB1_91:
	s_or_saveexec_b64 s[24:25], s[24:25]
	v_mov_b32_e32 v116, 0
	v_mov_b32_e32 v117, 0
	v_mov_b32_e32 v172, 0
	v_mov_b32_e32 v173, 0
	v_mov_b32_e32 v150, 0
	v_mov_b32_e32 v151, 0
	v_mov_b32_e32 v152, 0
	v_mov_b32_e32 v153, 0
	v_mov_b32_e32 v176, 0
	v_mov_b32_e32 v177, 0
	v_mov_b32_e32 v174, 0
	v_mov_b32_e32 v175, 0
	s_xor_b64 exec, exec, s[24:25]
	s_cbranch_execz .LBB1_93
	s_lshl_b32 s42, s46, 1
	v_add_u32_e32 v115, s42, v199
	v_mul_u32_u24_e32 v132, 0xe0, v233
	v_add_u32_e32 v115, s54, v132
	v_add_u32_e32 v162, 0xe00, v115
	v_add3_u32 v115, v162, v234, v235
	ds_read_b64 v[132:133], v115 offset:80
	v_mad_u32_u24 v115, v167, s52, v198
	ds_read_b128 v[150:153], v115 offset:60416
	s_waitcnt lgkmcnt(5)
	v_mfma_f32_16x16x32_bf16 v[240:243], v[86:89], v[146:149], 0
	s_waitcnt lgkmcnt(2)
	v_mfma_f32_16x16x32_bf16 v[116:119], v[250:253], v[146:149], v[120:123]
	v_mfma_f32_16x16x32_bf16 v[124:127], v[124:127], v[138:141], 0
	v_mfma_f32_16x16x32_bf16 v[118:121], v[246:249], v[142:145], v[116:119]
	v_mfma_f32_16x16x32_bf16 v[122:125], v[128:131], v[134:137], v[124:127]
	s_nop 0
	s_waitcnt lgkmcnt(1)
	v_lshlrev_b32_e32 v116, 16, v132
	v_and_b32_e32 v117, 0xffff0000, v132
	v_lshlrev_b32_e32 v172, 16, v133
	v_and_b32_e32 v173, 0xffff0000, v133
	v_mov_b32_e32 v115, s56
	s_nop 3
	v_pk_add_f32 v[174:175], v[120:121], v[124:125]
	v_pk_add_f32 v[176:177], v[118:119], v[122:123]
	v_sub_f32_e32 v119, 1.0, v117
	v_sub_f32_e32 v118, 1.0, v116
	v_sub_f32_e32 v121, 1.0, v173
	v_sub_f32_e32 v120, 1.0, v172
	v_pk_mul_f32 v[120:121], v[174:175], v[120:121]
	v_pk_mul_f32 v[118:119], v[176:177], v[118:119]
	s_waitcnt lgkmcnt(0)
	v_pk_fma_f32 v[122:123], v[152:153], v[172:173], v[120:121]
	v_pk_fma_f32 v[124:125], v[150:151], v[116:117], v[118:119]
	v_mfma_f32_16x16x32_bf16 v[118:121], v[2:5], v[146:149], 0
	v_cndmask_b32_e64 v115, v123, v115, s[14:15]
	v_cndmask_b32_e64 v123, v122, v122, s[14:15]
	v_cndmask_b32_e64 v122, v125, v125, s[14:15]
	v_cndmask_b32_e64 v124, v124, v124, s[14:15]
	v_cvt_pk_bf16_f32 v122, v124, v122
	v_cvt_pk_bf16_f32 v123, v123, v115
	ds_write_b64 v200, v[122:123] offset:58112
	s_and_saveexec_b64 s[72:73], s[18:19]
	v_mov_b32_e32 v115, 0xe380
	ds_add_u32 v115, v115
	s_or_b64 exec, exec, s[72:73]
	v_mfma_f32_16x16x32_bf16 v[118:121], v[6:9], v[142:145], v[118:121]
	v_lshl_add_u32 v115, v192, 1, v162
	ds_read_b128 v[130:133], v115 offset:128
	v_add_u32_e32 v115, s42, v228
	ds_read_b128 v[162:165], v115 offset:39168
	ds_read_b128 v[244:247], v115 offset:39232
	s_add_i32 s42, s33, 32
	s_and_b32 s42, s42, 0x60
	v_mfma_f32_16x16x32_bf16 v[118:121], v[10:13], v[138:141], v[118:121]
	v_or_b32_e32 v236, s42, v189
	v_mad_u32_u24 v248, v236, s3, v227
	ds_read_b128 v[236:239], v248
	v_mfma_f32_16x16x32_bf16 v[118:121], v[14:17], v[134:137], v[118:121]
	s_waitcnt lgkmcnt(0)
	v_mfma_f32_16x16x32_bf16 v[162:165], v[162:165], v[236:239], 0
	ds_read_b128 v[236:239], v248 offset:64
	v_mfma_f32_16x16x32_bf16 v[126:129], v[26:29], v[130:133], v[118:121]
	v_mfma_f32_16x16x32_bf16 v[118:121], v[30:33], v[146:149], 0
	v_mfma_f32_16x16x32_bf16 v[122:125], v[58:61], v[146:149], 0
	v_mfma_f32_16x16x32_bf16 v[118:121], v[34:37], v[142:145], v[118:121]
	v_mfma_f32_16x16x32_bf16 v[122:125], v[62:65], v[142:145], v[122:125]
	s_waitcnt lgkmcnt(0)
	v_mfma_f32_16x16x32_bf16 v[162:165], v[244:247], v[236:239], v[162:165]
	v_mov_b32_e32 v246, 0xe380
	ds_read_b32 v246, v246
	v_mfma_f32_16x16x32_bf16 v[236:239], v[90:93], v[142:145], v[240:243]
	v_mfma_f32_16x16x32_bf16 v[118:121], v[38:41], v[138:141], v[118:121]
	s_nop 5
	v_med3_f32 v115, v162, s55, 0
	v_exp_f32_e32 v162, v115
	v_med3_f32 v115, v163, s55, 0
	v_mfma_f32_16x16x32_bf16 v[122:125], v[66:69], v[138:141], v[122:125]
	v_exp_f32_e32 v163, v115
	v_med3_f32 v115, v164, s55, 0
	v_exp_f32_e32 v164, v115
	v_mfma_f32_16x16x32_bf16 v[236:239], v[94:97], v[138:141], v[236:239]
	v_med3_f32 v115, v165, s55, 0
	v_exp_f32_e32 v165, v115
	v_mfma_f32_16x16x32_bf16 v[118:121], v[42:45], v[134:137], v[118:121]
	v_mfma_f32_16x16x32_bf16 v[122:125], v[70:73], v[134:137], v[122:125]
	v_mfma_f32_16x16x32_bf16 v[236:239], v[98:101], v[134:137], v[236:239]
	v_mfma_f32_16x16x32_bf16 v[118:121], v[54:57], v[130:133], v[118:121]
	v_mfma_f32_16x16x32_bf16 v[122:125], v[82:85], v[130:133], v[122:125]
	v_mfma_f32_16x16x32_bf16 v[130:133], v[110:113], v[130:133], v[236:239]

.Lred_skip_1:
	s_nop 5
	v_exp_f32_e32 v115, v116
	v_med3_f32 v116, v120, s55, v232
	v_exp_f32_e32 v125, v116
	v_mfma_f32_16x16x32_bf16 v[130:133], v[102:105], v[134:137], v[130:133]
	v_med3_f32 v121, v121, s55, v232
	v_exp_f32_e32 v124, v126
	v_exp_f32_e32 v126, v127
	v_exp_f32_e32 v127, v121
	v_mfma_f32_16x16x32_bf16 v[130:133], v[106:109], v[138:141], v[130:133]
	v_exp_f32_e32 v117, v117
	v_add_f32_e32 v115, 1.0, v115
	v_pk_add_f32 v[134:135], v[124:125], 1.0 op_sel_hi:[1,0]
	v_rcp_f32_e32 v120, v115
	v_mul_f32_e32 v115, v134, v135
	v_pk_add_f32 v[134:135], v[126:127], 1.0 op_sel_hi:[1,0]
	s_nop 1
	v_exp_f32_e32 v116, v130
	v_rcp_f32_e32 v130, v115
	v_add_f32_e32 v115, 1.0, v117
	v_mul_f32_e32 v117, v134, v135
	v_exp_f32_e32 v124, v131
	v_rcp_f32_e32 v131, v117
	v_rcp_f32_e32 v121, v115
	v_mov_b32_e32 v126, v125
	v_pk_add_f32 v[126:127], v[126:127], 1.0 op_sel_hi:[1,0] neg_lo:[1,0] neg_hi:[1,0]
	v_med3_f32 v123, v123, s55, v232
	v_pk_mul_f32 v[126:127], v[126:127], v[130:131]
	v_exp_f32_e32 v119, v119
	v_pk_fma_f32 v[168:169], v[168:169], v[120:121], v[126:127]
	s_nop 0
	v_mul_f32_e32 v115, 0xc038aa3b, v168
	v_med3_f32 v115, v115, s55, v232
	v_exp_f32_e32 v117, v115
	v_mul_f32_e32 v115, 0xc038aa3b, v169
	v_med3_f32 v115, v115, s55, v232
	v_exp_f32_e32 v125, v115
	v_pk_add_f32 v[120:121], v[116:117], 1.0 op_sel_hi:[1,0]
	v_pk_add_f32 v[126:127], v[124:125], 1.0 op_sel_hi:[1,0]
	v_mul_f32_e32 v115, v120, v121
	v_rcp_f32_e32 v120, v115
	v_mul_f32_e32 v115, v126, v127
	v_rcp_f32_e32 v121, v115
	v_mov_b32_e32 v124, v117
	v_exp_f32_e32 v115, v118
	v_med3_f32 v118, v122, s55, v232
	v_pk_add_f32 v[116:117], v[124:125], 1.0 op_sel_hi:[1,0] neg_lo:[1,0] neg_hi:[1,0]
	v_exp_f32_e32 v124, v128
	v_exp_f32_e32 v125, v118
	v_add_f32_e32 v115, 1.0, v115
	v_rcp_f32_e32 v122, v115
	v_exp_f32_e32 v118, v132
	v_pk_add_f32 v[126:127], v[124:125], 1.0 op_sel_hi:[1,0]
	v_exp_f32_e32 v124, v133
	v_mul_f32_e32 v115, v126, v127
	v_exp_f32_e32 v126, v129
	v_exp_f32_e32 v127, v123
	v_rcp_f32_e32 v128, v115
	v_add_f32_e32 v115, 1.0, v119
	v_rcp_f32_e32 v123, v115
	v_pk_add_f32 v[130:131], v[126:127], 1.0 op_sel_hi:[1,0]
	v_mov_b32_e32 v126, v125
	v_mul_f32_e32 v119, v130, v131
	v_rcp_f32_e32 v129, v119
	v_pk_add_f32 v[126:127], v[126:127], 1.0 op_sel_hi:[1,0] neg_lo:[1,0] neg_hi:[1,0]
	v_pk_mul_f32 v[116:117], v[116:117], v[120:121]
	v_pk_mul_f32 v[126:127], v[126:127], v[128:129]
	s_nop 0
	v_pk_fma_f32 v[170:171], v[170:171], v[122:123], v[126:127]
	v_cvt_pk_bf16_f32 v120, v116, v117
	v_mul_f32_e32 v115, 0xc038aa3b, v170
	v_med3_f32 v115, v115, s55, v232
	v_exp_f32_e32 v119, v115
	v_mul_f32_e32 v115, 0xc038aa3b, v171
	v_med3_f32 v115, v115, s55, v232
	v_exp_f32_e32 v125, v115
	v_pk_add_f32 v[122:123], v[118:119], 1.0 op_sel_hi:[1,0]
	v_pk_mul_f32 v[116:117], v[162:163], v[116:117]
	v_mul_f32_e32 v115, v122, v123
	v_pk_add_f32 v[126:127], v[124:125], 1.0 op_sel_hi:[1,0]
	v_rcp_f32_e32 v122, v115
	v_mul_f32_e32 v115, v126, v127
	v_rcp_f32_e32 v123, v115
	v_mov_b32_e32 v124, v119
	v_pk_add_f32 v[118:119], v[124:125], 1.0 op_sel_hi:[1,0] neg_lo:[1,0] neg_hi:[1,0]
	v_cvt_pk_bf16_f32 v116, v116, v117
	v_pk_mul_f32 v[118:119], v[118:119], v[122:123]
	v_add_u32_e32 v122, 0x80, v166
	v_cvt_pk_bf16_f32 v121, v118, v119
	v_mov_b32_e32 v123, v114
	v_pk_mul_f32 v[118:119], v[164:165], v[118:119]
	v_lshl_add_u64 v[122:123], v[122:123], 1, s[30:31]
	v_cvt_pk_bf16_f32 v117, v118, v119
	global_store_dwordx2 v[122:123], v[120:121], off nt
	ds_write_b64 v205, v[116:117]
	s_and_b64 s[72:73], exec, s[6:7]
	s_cbranch_scc1 .Lpf_skip_2
	ds_read_b128 v[250:253], v199 offset:9216
	ds_read_b128 v[120:123], v198 offset:57600
	ds_read_b128 v[124:127], v199 offset:9344
	ds_read_b128 v[246:249], v199 offset:9280
	ds_read_b128 v[128:131], v199 offset:9408
.Lpf_skip_2:
	s_waitcnt lgkmcnt(0)
	s_barrier
	ds_read_b128 v[146:149], v193
	ds_read_b128 v[142:145], v193 offset:64
	ds_read_b128 v[138:141], v193 offset:128
	ds_read_b128 v[134:137], v193 offset:192
	s_and_saveexec_b64 s[24:25], s[6:7]
	s_xor_b64 s[24:25], exec, s[24:25]
	s_cbranch_execz .LBB1_127
	s_and_saveexec_b64 s[42:43], s[8:9]
	s_xor_b64 s[42:43], exec, s[42:43]
	s_cbranch_execz .LBB1_124
	s_cmpk_eq_i32 s40, 0x1810
	s_cbranch_scc1 .LBB1_124
	s_bitcmp1_b32 s59, 0
	s_cselect_b32 s47, 0, 0x1c00
	s_waitcnt vmcnt(4)
	v_cvt_pk_bf16_f32 v115, v188, s0
	v_lshl_add_u32 v116, s47, 1, v223
	ds_write_b16 v116, v115 offset:80
	ds_write_b16 v213, v115 offset:80
	s_waitcnt vmcnt(3)
	v_cvt_pk_bf16_f32 v115, v187, s0
	ds_write_b16 v116, v115 offset:3664
	ds_write_b16 v215, v115 offset:80
	s_waitcnt vmcnt(2)
	v_cvt_pk_bf16_f32 v115, v186, s0
	ds_write_b16 v116, v115 offset:7248
	ds_write_b16 v216, v115 offset:80
	s_waitcnt vmcnt(1)
	v_cvt_pk_bf16_f32 v115, v157, s0
	ds_write_b16 v116, v115 offset:10832
	ds_write_b16 v217, v115 offset:80
	s_and_saveexec_b64 s[44:45], s[26:27]
	s_cbranch_execz .LBB1_121
	v_cvt_pk_bf16_f32 v115, v155, s0
	v_lshl_add_u32 v116, s47, 1, v224
	ds_write_b16 v116, v115 offset:80
	ds_write_b16 v214, v115 offset:80
	v_cvt_pk_bf16_f32 v115, v182, s0
	ds_write_b16 v116, v115 offset:3664
	ds_write_b16 v218, v115 offset:80
	v_cvt_pk_bf16_f32 v115, v183, s0
	ds_write_b16 v116, v115 offset:7248
	ds_write_b16 v219, v115 offset:80
	v_cvt_pk_bf16_f32 v115, v184, s0
	ds_write_b16 v116, v115 offset:10832
	ds_write_b16 v220, v115 offset:80

.LBB1_127:
	s_or_saveexec_b64 s[24:25], s[24:25]
	v_mov_b32_e32 v116, 0
	v_mov_b32_e32 v117, 0
	v_mov_b32_e32 v172, 0
	v_mov_b32_e32 v173, 0
	v_mov_b32_e32 v150, 0
	v_mov_b32_e32 v151, 0
	v_mov_b32_e32 v152, 0
	v_mov_b32_e32 v153, 0
	v_mov_b32_e32 v176, 0
	v_mov_b32_e32 v177, 0
	v_mov_b32_e32 v174, 0
	v_mov_b32_e32 v175, 0
	s_xor_b64 exec, exec, s[24:25]
	s_cbranch_execz .LBB1_129
	s_lshl_b32 s42, s46, 1
	v_add_u32_e32 v115, s42, v199
	v_mul_u32_u24_e32 v132, 0xe0, v167
	v_add_u32_e32 v115, s54, v132
	v_add_u32_e32 v162, 0xe00, v115
	v_add3_u32 v115, v162, v234, v235
	ds_read_b64 v[132:133], v115 offset:80
	v_mad_u32_u24 v115, v236, s52, v198
	ds_read_b128 v[150:153], v115 offset:60416
	s_waitcnt lgkmcnt(5)
	v_mfma_f32_16x16x32_bf16 v[242:245], v[86:89], v[146:149], 0
	s_waitcnt lgkmcnt(2)
	v_mfma_f32_16x16x32_bf16 v[116:119], v[250:253], v[146:149], v[120:123]
	v_mfma_f32_16x16x32_bf16 v[124:127], v[124:127], v[138:141], 0
	v_mfma_f32_16x16x32_bf16 v[118:121], v[246:249], v[142:145], v[116:119]
	v_mfma_f32_16x16x32_bf16 v[122:125], v[128:131], v[134:137], v[124:127]
	s_nop 0
	s_waitcnt lgkmcnt(1)
	v_lshlrev_b32_e32 v116, 16, v132
	v_and_b32_e32 v117, 0xffff0000, v132
	v_lshlrev_b32_e32 v172, 16, v133
	v_and_b32_e32 v173, 0xffff0000, v133
	v_mov_b32_e32 v115, s56
	s_nop 3
	v_pk_add_f32 v[174:175], v[120:121], v[124:125]
	v_pk_add_f32 v[176:177], v[118:119], v[122:123]
	v_sub_f32_e32 v119, 1.0, v117
	v_sub_f32_e32 v118, 1.0, v116
	v_sub_f32_e32 v121, 1.0, v173
	v_sub_f32_e32 v120, 1.0, v172
	v_pk_mul_f32 v[120:121], v[174:175], v[120:121]
	v_pk_mul_f32 v[118:119], v[176:177], v[118:119]
	s_waitcnt lgkmcnt(0)
	v_pk_fma_f32 v[122:123], v[152:153], v[172:173], v[120:121]
	v_pk_fma_f32 v[124:125], v[150:151], v[116:117], v[118:119]
	v_mfma_f32_16x16x32_bf16 v[118:121], v[2:5], v[146:149], 0
	v_cndmask_b32_e64 v115, v123, v115, s[14:15]
	v_cndmask_b32_e64 v123, v122, v122, s[14:15]
	v_cndmask_b32_e64 v122, v125, v125, s[14:15]
	v_cndmask_b32_e64 v124, v124, v124, s[14:15]
	v_cvt_pk_bf16_f32 v122, v124, v122
	v_cvt_pk_bf16_f32 v123, v123, v115
	ds_write_b64 v200, v[122:123] offset:58112
	s_and_saveexec_b64 s[72:73], s[18:19]
	v_mov_b32_e32 v115, 0xe380
	ds_add_u32 v115, v115
	s_or_b64 exec, exec, s[72:73]
	v_mfma_f32_16x16x32_bf16 v[118:121], v[6:9], v[142:145], v[118:121]
	v_lshl_add_u32 v115, v192, 1, v162
	ds_read_b128 v[130:133], v115 offset:128
	v_add_u32_e32 v115, s42, v228
	ds_read_b128 v[162:165], v115 offset:39168
	ds_read_b128 v[246:249], v115 offset:39232
	s_add_i32 s42, s33, 32
	s_and_b32 s42, s42, 0x60
	v_mfma_f32_16x16x32_bf16 v[118:121], v[10:13], v[138:141], v[118:121]
	v_or_b32_e32 v167, s42, v189
	v_mad_u32_u24 v167, v167, s3, v227
	ds_read_b128 v[238:241], v167 offset:2304
	v_mfma_f32_16x16x32_bf16 v[118:121], v[14:17], v[134:137], v[118:121]
	s_waitcnt lgkmcnt(0)
	v_mfma_f32_16x16x32_bf16 v[162:165], v[162:165], v[238:241], 0
	ds_read_b128 v[238:241], v167 offset:2368
	v_mfma_f32_16x16x32_bf16 v[126:129], v[26:29], v[130:133], v[118:121]
	v_mfma_f32_16x16x32_bf16 v[118:121], v[30:33], v[146:149], 0
	v_mfma_f32_16x16x32_bf16 v[122:125], v[58:61], v[146:149], 0
	v_mfma_f32_16x16x32_bf16 v[118:121], v[34:37], v[142:145], v[118:121]
	v_mfma_f32_16x16x32_bf16 v[122:125], v[62:65], v[142:145], v[122:125]
	s_waitcnt lgkmcnt(0)
	v_mfma_f32_16x16x32_bf16 v[162:165], v[246:249], v[238:241], v[162:165]
	v_mov_b32_e32 v246, 0xe380
	ds_read_b32 v246, v246
	v_mfma_f32_16x16x32_bf16 v[238:241], v[90:93], v[142:145], v[242:245]
	v_mfma_f32_16x16x32_bf16 v[118:121], v[38:41], v[138:141], v[118:121]
	s_nop 5
	v_med3_f32 v115, v162, s55, 0
	v_exp_f32_e32 v162, v115
	v_med3_f32 v115, v163, s55, 0
	v_mfma_f32_16x16x32_bf16 v[122:125], v[66:69], v[138:141], v[122:125]
	v_exp_f32_e32 v163, v115
	v_med3_f32 v115, v164, s55, 0
	v_exp_f32_e32 v164, v115
	v_mfma_f32_16x16x32_bf16 v[238:241], v[94:97], v[138:141], v[238:241]
	v_med3_f32 v115, v165, s55, 0
	v_exp_f32_e32 v165, v115
	v_mfma_f32_16x16x32_bf16 v[118:121], v[42:45], v[134:137], v[118:121]
	v_mfma_f32_16x16x32_bf16 v[122:125], v[70:73], v[134:137], v[122:125]
	v_mfma_f32_16x16x32_bf16 v[238:241], v[98:101], v[134:137], v[238:241]
	v_mfma_f32_16x16x32_bf16 v[118:121], v[54:57], v[130:133], v[118:121]
	v_mfma_f32_16x16x32_bf16 v[122:125], v[82:85], v[130:133], v[122:125]
	v_mfma_f32_16x16x32_bf16 v[130:133], v[110:113], v[130:133], v[238:241]

.Lred_skip_2:
	s_nop 5
	v_exp_f32_e32 v115, v116
	v_med3_f32 v116, v120, s55, v232
	v_exp_f32_e32 v125, v116
	v_mfma_f32_16x16x32_bf16 v[130:133], v[102:105], v[134:137], v[130:133]
	v_med3_f32 v121, v121, s55, v232
	v_exp_f32_e32 v124, v126
	v_exp_f32_e32 v126, v127
	v_exp_f32_e32 v127, v121
	v_mfma_f32_16x16x32_bf16 v[130:133], v[106:109], v[138:141], v[130:133]
	v_exp_f32_e32 v117, v117
	v_add_f32_e32 v115, 1.0, v115
	v_pk_add_f32 v[134:135], v[124:125], 1.0 op_sel_hi:[1,0]
	v_rcp_f32_e32 v120, v115
	v_mul_f32_e32 v115, v134, v135
	v_pk_add_f32 v[134:135], v[126:127], 1.0 op_sel_hi:[1,0]
	s_nop 1
	v_exp_f32_e32 v116, v130
	v_rcp_f32_e32 v130, v115
	v_add_f32_e32 v115, 1.0, v117
	v_mul_f32_e32 v117, v134, v135
	v_exp_f32_e32 v124, v131
	v_rcp_f32_e32 v131, v117
	v_rcp_f32_e32 v121, v115
	v_mov_b32_e32 v126, v125
	v_pk_add_f32 v[126:127], v[126:127], 1.0 op_sel_hi:[1,0] neg_lo:[1,0] neg_hi:[1,0]
	v_med3_f32 v123, v123, s55, v232
	v_pk_mul_f32 v[126:127], v[126:127], v[130:131]
	v_exp_f32_e32 v119, v119
	v_pk_fma_f32 v[168:169], v[168:169], v[120:121], v[126:127]
	s_nop 0
	v_mul_f32_e32 v115, 0xc038aa3b, v168
	v_med3_f32 v115, v115, s55, v232
	v_exp_f32_e32 v117, v115
	v_mul_f32_e32 v115, 0xc038aa3b, v169
	v_med3_f32 v115, v115, s55, v232
	v_exp_f32_e32 v125, v115
	v_pk_add_f32 v[120:121], v[116:117], 1.0 op_sel_hi:[1,0]
	v_pk_add_f32 v[126:127], v[124:125], 1.0 op_sel_hi:[1,0]
	v_mul_f32_e32 v115, v120, v121
	v_rcp_f32_e32 v120, v115
	v_mul_f32_e32 v115, v126, v127
	v_rcp_f32_e32 v121, v115
	v_mov_b32_e32 v124, v117
	v_exp_f32_e32 v115, v118
	v_med3_f32 v118, v122, s55, v232
	v_pk_add_f32 v[116:117], v[124:125], 1.0 op_sel_hi:[1,0] neg_lo:[1,0] neg_hi:[1,0]
	v_exp_f32_e32 v124, v128
	v_exp_f32_e32 v125, v118
	v_add_f32_e32 v115, 1.0, v115
	v_rcp_f32_e32 v122, v115
	v_exp_f32_e32 v118, v132
	v_pk_add_f32 v[126:127], v[124:125], 1.0 op_sel_hi:[1,0]
	v_exp_f32_e32 v124, v133
	v_mul_f32_e32 v115, v126, v127
	v_exp_f32_e32 v126, v129
	v_exp_f32_e32 v127, v123
	v_rcp_f32_e32 v128, v115
	v_add_f32_e32 v115, 1.0, v119
	v_rcp_f32_e32 v123, v115
	v_pk_add_f32 v[130:131], v[126:127], 1.0 op_sel_hi:[1,0]
	v_mov_b32_e32 v126, v125
	v_mul_f32_e32 v119, v130, v131
	v_rcp_f32_e32 v129, v119
	v_pk_add_f32 v[126:127], v[126:127], 1.0 op_sel_hi:[1,0] neg_lo:[1,0] neg_hi:[1,0]
	v_pk_mul_f32 v[116:117], v[116:117], v[120:121]
	v_pk_mul_f32 v[126:127], v[126:127], v[128:129]
	s_nop 0
	v_pk_fma_f32 v[170:171], v[170:171], v[122:123], v[126:127]
	v_cvt_pk_bf16_f32 v120, v116, v117
	v_mul_f32_e32 v115, 0xc038aa3b, v170
	v_med3_f32 v115, v115, s55, v232
	v_exp_f32_e32 v119, v115
	v_mul_f32_e32 v115, 0xc038aa3b, v171
	v_med3_f32 v115, v115, s55, v232
	v_exp_f32_e32 v125, v115
	v_pk_add_f32 v[122:123], v[118:119], 1.0 op_sel_hi:[1,0]
	v_pk_mul_f32 v[116:117], v[162:163], v[116:117]
	v_mul_f32_e32 v115, v122, v123
	v_pk_add_f32 v[126:127], v[124:125], 1.0 op_sel_hi:[1,0]
	v_rcp_f32_e32 v122, v115
	v_mul_f32_e32 v115, v126, v127
	v_rcp_f32_e32 v123, v115
	v_mov_b32_e32 v124, v119
	v_pk_add_f32 v[118:119], v[124:125], 1.0 op_sel_hi:[1,0] neg_lo:[1,0] neg_hi:[1,0]
	v_cvt_pk_bf16_f32 v116, v116, v117
	v_pk_mul_f32 v[118:119], v[118:119], v[122:123]
	v_add_u32_e32 v122, 0x100, v166
	v_cvt_pk_bf16_f32 v121, v118, v119
	v_mov_b32_e32 v123, v114
	v_pk_mul_f32 v[118:119], v[164:165], v[118:119]
	v_lshl_add_u64 v[122:123], v[122:123], 1, s[30:31]
	v_cvt_pk_bf16_f32 v117, v118, v119
	global_store_dwordx2 v[122:123], v[120:121], off nt
	ds_write_b64 v205, v[116:117] offset:4608
	s_and_b64 s[72:73], exec, s[6:7]
	s_cbranch_scc1 .Lpf_skip_3
	ds_read_b128 v[250:253], v199 offset:9216
	ds_read_b128 v[120:123], v198 offset:57600
	ds_read_b128 v[124:127], v199 offset:9344
	ds_read_b128 v[246:249], v199 offset:9280
	ds_read_b128 v[128:131], v199 offset:9408
.Lpf_skip_3:
	s_waitcnt lgkmcnt(0)
	s_barrier
	ds_read_b128 v[134:137], v206 offset:4608
	ds_read_b128 v[138:141], v206 offset:4672
	ds_read_b128 v[142:145], v206 offset:4736
	ds_read_b128 v[146:149], v206 offset:4800
	s_and_saveexec_b64 s[42:43], s[6:7]
	s_xor_b64 s[42:43], exec, s[42:43]
	s_cbranch_execz .LBB1_165
	s_and_saveexec_b64 s[44:45], s[8:9]
	s_xor_b64 s[44:45], exec, s[44:45]
	s_cbranch_execz .LBB1_160
	s_andn2_b64 vcc, exec, s[24:25]
	s_cbranch_vccnz .LBB1_160
	s_andn2_b32 s49, 1, s59
	s_mulk_i32 s49, 0xd00
	v_lshl_add_u32 v115, s49, 2, v185
	v_add_u32_e32 v116, 0xec00, v115
	s_waitcnt vmcnt(3)
	ds_write2st64_b32 v115, v188, v187 offset0:236 offset1:249
	s_waitcnt vmcnt(1)
	ds_write2st64_b32 v116, v186, v157 offset0:26 offset1:39
	s_and_saveexec_b64 s[46:47], s[26:27]
	s_cbranch_execz .LBB1_194
	v_lshl_add_u32 v115, s49, 2, v225
	v_add_u32_e32 v116, 0xec00, v115
	ds_write2st64_b32 v115, v155, v182 offset0:236 offset1:249
	ds_write2st64_b32 v116, v183, v184 offset0:26 offset1:39
	s_or_b64 exec, exec, s[46:47]
	s_and_saveexec_b64 s[46:47], s[20:21]
	s_cbranch_execnz .LBB1_195

.LBB1_165:
	s_or_saveexec_b64 s[42:43], s[42:43]
	v_cndmask_b32_e64 v115, 0, 1, s[24:25]
	v_mov_b32_e32 v117, 0
	v_cmp_ne_u32_e64 s[24:25], 1, v115
	v_mov_b32_e32 v116, 0
	v_mov_b32_e32 v177, 0
	v_mov_b32_e32 v176, 0
	v_mov_b32_e32 v153, 0
	v_mov_b32_e32 v152, 0
	v_mov_b32_e32 v151, 0
	v_mov_b32_e32 v150, 0
	v_mov_b32_e32 v173, 0
	v_mov_b32_e32 v172, 0
	v_mov_b32_e32 v175, 0
	v_mov_b32_e32 v174, 0
	s_xor_b64 exec, exec, s[42:43]
	s_cbranch_execz .LBB1_169
	v_lshl_add_u32 v115, s48, 1, v199
	v_mul_u32_u24_e32 v132, 0xe0, v236
	s_and_b64 vcc, exec, s[24:25]
	v_add_u32_e32 v115, s54, v132
	v_add_u32_e32 v132, 0xe00, v115
	v_add3_u32 v115, v132, v234, v235
	s_waitcnt lgkmcnt(0)
	v_mfma_f32_16x16x32_bf16 v[124:127], v[124:127], v[142:145], 0
	v_mfma_f32_16x16x32_bf16 v[116:119], v[250:253], v[134:137], v[120:123]
	v_mfma_f32_16x16x32_bf16 v[118:121], v[246:249], v[138:141], v[116:119]
	s_nop 2
	ds_read_b64 v[116:117], v115 offset:80
	v_mad_u32_u24 v115, v167, s52, v198
	ds_read_b128 v[150:153], v115 offset:60416
	v_mfma_f32_16x16x32_bf16 v[122:125], v[128:131], v[146:149], v[124:127]
	v_mov_b32_e32 v115, s56
	s_waitcnt lgkmcnt(1)
	v_lshlrev_b32_e32 v174, 16, v116
	v_and_b32_e32 v175, 0xffff0000, v116
	v_lshlrev_b32_e32 v172, 16, v117
	v_and_b32_e32 v173, 0xffff0000, v117
	s_nop 1
	v_pk_add_f32 v[116:117], v[120:121], v[124:125]
	v_pk_add_f32 v[176:177], v[118:119], v[122:123]
	v_sub_f32_e32 v119, 1.0, v173
	v_sub_f32_e32 v118, 1.0, v172
	v_sub_f32_e32 v121, 1.0, v175
	v_sub_f32_e32 v120, 1.0, v174
	v_pk_mul_f32 v[120:121], v[176:177], v[120:121]
	v_pk_mul_f32 v[118:119], v[116:117], v[118:119]
	s_waitcnt lgkmcnt(0)
	v_pk_fma_f32 v[124:125], v[150:151], v[174:175], v[120:121]
	v_pk_fma_f32 v[122:123], v[152:153], v[172:173], v[118:119]
	v_cndmask_b32_e64 v124, v124, v124, s[14:15]
	v_cndmask_b32_e64 v115, v123, v115, s[14:15]
	v_cndmask_b32_e64 v123, v122, v122, s[14:15]
	v_cndmask_b32_e64 v122, v125, v125, s[14:15]
	v_cvt_pk_bf16_f32 v122, v124, v122
	v_cvt_pk_bf16_f32 v123, v123, v115
	v_mfma_f32_16x16x32_bf16 v[118:121], v[2:5], v[134:137], 0
	ds_write_b64 v200, v[122:123] offset:58112
	s_and_saveexec_b64 s[72:73], s[18:19]
	v_mov_b32_e32 v115, 0xe380
	ds_add_u32 v115, v115
	s_or_b64 exec, exec, s[72:73]
	v_lshl_add_u32 v115, v192, 1, v132
	v_mfma_f32_16x16x32_bf16 v[122:125], v[30:33], v[134:137], 0
	ds_read_b128 v[130:133], v115 offset:128
	v_mfma_f32_16x16x32_bf16 v[126:129], v[58:61], v[134:137], 0
	v_mfma_f32_16x16x32_bf16 v[234:237], v[86:89], v[134:137], 0
	v_mfma_f32_16x16x32_bf16 v[118:121], v[6:9], v[138:141], v[118:121]
	v_mfma_f32_16x16x32_bf16 v[122:125], v[34:37], v[138:141], v[122:125]
	v_mfma_f32_16x16x32_bf16 v[126:129], v[62:65], v[138:141], v[126:129]
	v_mfma_f32_16x16x32_bf16 v[234:237], v[90:93], v[138:141], v[234:237]
	v_mfma_f32_16x16x32_bf16 v[118:121], v[10:13], v[142:145], v[118:121]
	v_mfma_f32_16x16x32_bf16 v[122:125], v[38:41], v[142:145], v[122:125]
	v_mfma_f32_16x16x32_bf16 v[126:129], v[66:69], v[142:145], v[126:129]
	v_mfma_f32_16x16x32_bf16 v[234:237], v[94:97], v[142:145], v[234:237]
	v_mfma_f32_16x16x32_bf16 v[118:121], v[14:17], v[146:149], v[118:121]
	v_mfma_f32_16x16x32_bf16 v[122:125], v[42:45], v[146:149], v[122:125]
	v_mfma_f32_16x16x32_bf16 v[126:129], v[70:73], v[146:149], v[126:129]
	v_mfma_f32_16x16x32_bf16 v[234:237], v[98:101], v[146:149], v[234:237]
	s_waitcnt lgkmcnt(0)
	v_mfma_f32_16x16x32_bf16 v[118:121], v[26:29], v[130:133], v[118:121]
	v_mov_b32_e32 v246, 0xe380
	ds_read_b32 v246, v246
	v_mfma_f32_16x16x32_bf16 v[122:125], v[54:57], v[130:133], v[122:125]
	v_mfma_f32_16x16x32_bf16 v[126:129], v[82:85], v[130:133], v[126:129]
	v_mfma_f32_16x16x32_bf16 v[130:133], v[110:113], v[130:133], v[234:237]
	s_cbranch_vccnz .LBB1_168
	v_lshl_add_u32 v115, s48, 1, v228
	ds_read_b128 v[162:165], v115 offset:39168
	s_add_i32 s44, s33, 64
	v_and_or_b32 v233, s44, 64, v189
	v_mad_u32_u24 v233, v233, s3, v227
	ds_read_b128 v[234:237], v115 offset:39232
	ds_read_b128 v[238:241], v233
	ds_read_b128 v[242:245], v233 offset:64
	s_waitcnt lgkmcnt(1)
	v_mfma_f32_16x16x32_bf16 v[162:165], v[162:165], v[238:241], 0
	s_waitcnt lgkmcnt(0)
	v_mfma_f32_16x16x32_bf16 v[162:165], v[234:237], v[242:245], v[162:165]
	s_nop 7
	v_med3_f32 v115, v162, s55, 0
	v_med3_f32 v163, v163, s55, 0
	v_med3_f32 v164, v164, s55, 0
	v_med3_f32 v165, v165, s55, 0
	v_exp_f32_e32 v162, v115
	v_exp_f32_e32 v163, v163
	v_exp_f32_e32 v164, v164
	v_exp_f32_e32 v165, v165

	.amdhsa_kernel _Z10rnn_kernelPKfS0_S0_S0_S0_S0_PKtS2_PfPtS3_
		.amdhsa_group_segment_fixed_size 0
		.amdhsa_private_segment_fixed_size 0
		.amdhsa_kernarg_size 88
		.amdhsa_user_sgpr_count 2
		.amdhsa_user_sgpr_dispatch_ptr 0
		.amdhsa_user_sgpr_queue_ptr 0
		.amdhsa_user_sgpr_kernarg_segment_ptr 1
		.amdhsa_user_sgpr_dispatch_id 0
		.amdhsa_user_sgpr_kernarg_preload_length 0
		.amdhsa_user_sgpr_kernarg_preload_offset 0
		.amdhsa_user_sgpr_private_segment_size 0
		.amdhsa_uses_dynamic_stack 0
		.amdhsa_enable_private_segment 0
		.amdhsa_system_sgpr_workgroup_id_x 1
		.amdhsa_system_sgpr_workgroup_id_y 0
		.amdhsa_system_sgpr_workgroup_id_z 0
		.amdhsa_system_sgpr_workgroup_info 0
		.amdhsa_system_vgpr_workitem_id 0
		.amdhsa_next_free_vgpr 256
		.amdhsa_next_free_sgpr 76
		.amdhsa_accum_offset 256
		.amdhsa_reserve_vcc 1
		.amdhsa_float_round_mode_32 0
		.amdhsa_float_round_mode_16_64 0
		.amdhsa_float_denorm_mode_32 3
		.amdhsa_float_denorm_mode_16_64 3
		.amdhsa_dx10_clamp 1
		.amdhsa_ieee_mode 1
		.amdhsa_fp16_overflow 0
		.amdhsa_tg_split 0
		.amdhsa_exception_fp_ieee_invalid_op 0
		.amdhsa_exception_fp_denorm_src 0
		.amdhsa_exception_fp_ieee_div_zero 0
		.amdhsa_exception_fp_ieee_overflow 0
		.amdhsa_exception_fp_ieee_underflow 0
		.amdhsa_exception_fp_ieee_inexact 0
		.amdhsa_exception_int_div_zero 0
	.end_amdhsa_kernel

amdhsa.kernels:
  - .agpr_count:     0
    .args:
      - .actual_access:  read_only
        .address_space:  global
        .offset:         0
        .size:           8
        .value_kind:     global_buffer
      - .actual_access:  read_only
        .address_space:  global
        .offset:         8
        .size:           8
        .value_kind:     global_buffer
      - .actual_access:  read_only
        .address_space:  global
        .offset:         16
        .size:           8
        .value_kind:     global_buffer
      - .actual_access:  read_only
        .address_space:  global
        .offset:         24
        .size:           8
        .value_kind:     global_buffer
      - .actual_access:  read_only
        .address_space:  global
        .offset:         32
        .size:           8
        .value_kind:     global_buffer
      - .actual_access:  read_only
        .address_space:  global
        .offset:         40
        .size:           8
        .value_kind:     global_buffer
      - .actual_access:  read_only
        .address_space:  global
        .offset:         48
        .size:           8
        .value_kind:     global_buffer
      - .actual_access:  read_only
        .address_space:  global
        .offset:         56
        .size:           8
        .value_kind:     global_buffer
      - .actual_access:  read_only
        .address_space:  global
        .offset:         64
        .size:           8
        .value_kind:     global_buffer
      - .actual_access:  read_only
        .address_space:  global
        .offset:         72
        .size:           8
        .value_kind:     global_buffer
      - .actual_access:  read_only
        .address_space:  global
        .offset:         80
        .size:           8
        .value_kind:     global_buffer
      - .actual_access:  read_only
        .address_space:  global
        .offset:         88
        .size:           8
        .value_kind:     global_buffer
      - .actual_access:  read_only
        .address_space:  global
        .offset:         96
        .size:           8
        .value_kind:     global_buffer
      - .actual_access:  read_only
        .address_space:  global
        .offset:         104
        .size:           8
        .value_kind:     global_buffer
      - .actual_access:  read_only
        .address_space:  global
        .offset:         112
        .size:           8
        .value_kind:     global_buffer
      - .actual_access:  read_only
        .address_space:  global
        .offset:         120
        .size:           8
        .value_kind:     global_buffer
      - .actual_access:  write_only
        .address_space:  global
        .offset:         128
        .size:           8
        .value_kind:     global_buffer
      - .actual_access:  write_only
        .address_space:  global
        .offset:         136
        .size:           8
        .value_kind:     global_buffer
      - .actual_access:  write_only
        .address_space:  global
        .offset:         144
        .size:           8
        .value_kind:     global_buffer
    .group_segment_fixed_size: 0
    .kernarg_segment_align: 8
    .kernarg_segment_size: 152
    .language:       OpenCL C
    .language_version:
      - 2
      - 0
    .max_flat_workgroup_size: 256
    .name:           _Z11prep_kernelPKfS0_S0_S0_S0_S0_S0_S0_S0_S0_S0_S0_S0_S0_S0_S0_PtS1_S1_
    .private_segment_fixed_size: 0
    .sgpr_count:     30
    .sgpr_spill_count: 0
    .symbol:         _Z11prep_kernelPKfS0_S0_S0_S0_S0_S0_S0_S0_S0_S0_S0_S0_S0_S0_S0_PtS1_S1_.kd
    .uniform_work_group_size: 1
    .uses_dynamic_stack: false
    .vgpr_count:     8
    .vgpr_spill_count: 0
    .wavefront_size: 64
  - .agpr_count:     0
    .args:
      - .actual_access:  read_only
        .address_space:  global
        .offset:         0
        .size:           8
        .value_kind:     global_buffer
      - .actual_access:  read_only
        .address_space:  global
        .offset:         8
        .size:           8
        .value_kind:     global_buffer
      - .actual_access:  read_only
        .address_space:  global
        .offset:         16
        .size:           8
        .value_kind:     global_buffer
      - .actual_access:  read_only
        .address_space:  global
        .offset:         24
        .size:           8
        .value_kind:     global_buffer
      - .actual_access:  read_only
        .address_space:  global
        .offset:         32
        .size:           8
        .value_kind:     global_buffer
      - .actual_access:  read_only
        .address_space:  global
        .offset:         40
        .size:           8
        .value_kind:     global_buffer
      - .actual_access:  read_only
        .address_space:  global
        .offset:         48
        .size:           8
        .value_kind:     global_buffer
      - .actual_access:  read_only
        .address_space:  global
        .offset:         56
        .size:           8
        .value_kind:     global_buffer
      - .actual_access:  write_only
        .address_space:  global
        .offset:         64
        .size:           8
        .value_kind:     global_buffer
      - .actual_access:  write_only
        .address_space:  global
        .offset:         72
        .size:           8
        .value_kind:     global_buffer
      - .actual_access:  write_only
        .address_space:  global
        .offset:         80
        .size:           8
        .value_kind:     global_buffer
    .group_segment_fixed_size: 0
    .kernarg_segment_align: 8
    .kernarg_segment_size: 88
    .language:       OpenCL C
    .language_version:
      - 2
      - 0
    .max_flat_workgroup_size: 512
    .name:           _Z10rnn_kernelPKfS0_S0_S0_S0_S0_PKtS2_PfPtS3_
    .private_segment_fixed_size: 0
    .sgpr_count:     82
    .sgpr_spill_count: 0
    .symbol:         _Z10rnn_kernelPKfS0_S0_S0_S0_S0_PKtS2_PfPtS3_.kd
    .uniform_work_group_size: 1
    .uses_dynamic_stack: false
    .vgpr_count:     256
    .vgpr_spill_count: 0
    .wavefront_size: 64
  - .agpr_count:     0
    .args:
      - .actual_access:  read_only
        .address_space:  global
        .offset:         0
        .size:           8
        .value_kind:     global_buffer
      - .actual_access:  read_only
        .address_space:  global
        .offset:         8
        .size:           8
        .value_kind:     global_buffer
      - .actual_access:  read_only
        .address_space:  global
        .offset:         16
        .size:           8
        .value_kind:     global_buffer
      - .actual_access:  read_only
        .address_space:  global
        .offset:         24
        .size:           8
        .value_kind:     global_buffer
      - .actual_access:  read_only
        .address_space:  global
        .offset:         32
        .size:           8
        .value_kind:     global_buffer
      - .actual_access:  write_only
        .address_space:  global
        .offset:         40
        .size:           8
        .value_kind:     global_buffer
      - .actual_access:  write_only
        .address_space:  global
        .offset:         48
        .size:           8
        .value_kind:     global_buffer
    .group_segment_fixed_size: 0
    .kernarg_segment_align: 8
    .kernarg_segment_size: 56
    .language:       OpenCL C
    .language_version:
      - 2
      - 0
    .max_flat_workgroup_size: 1024
    .name:           _Z11attn_kernelPKtS0_PKfS2_S2_PfS3_
    .private_segment_fixed_size: 0
    .sgpr_count:     30
    .sgpr_spill_count: 0
    .symbol:         _Z11attn_kernelPKtS0_PKfS2_S2_PfS3_.kd
    .uniform_work_group_size: 1
    .uses_dynamic_stack: false
    .vgpr_count:     124
    .vgpr_spill_count: 0
    .wavefront_size: 64
  - .agpr_count:     0
    .args:
      - .actual_access:  read_only
        .address_space:  global
        .offset:         0
        .size:           8
        .value_kind:     global_buffer
      - .actual_access:  read_only
        .address_space:  global
        .offset:         8
        .size:           8
        .value_kind:     global_buffer
      - .actual_access:  read_only
        .address_space:  global
        .offset:         16
        .size:           8
        .value_kind:     global_buffer
      - .actual_access:  write_only
        .address_space:  global
        .offset:         24
        .size:           8
        .value_kind:     global_buffer
    .group_segment_fixed_size: 192
    .kernarg_segment_align: 8
    .kernarg_segment_size: 32
    .language:       OpenCL C
    .language_version:
      - 2
      - 0
    .max_flat_workgroup_size: 1024
    .name:           _Z11loss_kernelPKfS0_S0_Pf
    .private_segment_fixed_size: 0
    .sgpr_count:     14
    .sgpr_spill_count: 0
    .symbol:         _Z11loss_kernelPKfS0_S0_Pf.kd
    .uniform_work_group_size: 1
    .uses_dynamic_stack: false
    .vgpr_count:     46
    .vgpr_spill_count: 0
    .wavefront_size: 64
